# cache policy: nt (non-temporal) on the weight-conversion's once-read f32 LDS-DMA loads, so the stream does not evict the GEMM operands from L2
# baseline (speedup 1.0000x reference)
; #define LAS __attribute__((address_space(3)))
; __device__ __forceinline__ void cvt_issue(const CvtD& d, int lane, LAS unsigned char* buf, LAS unsigned char* shb) {
;     ...
;     const float* base = d.W + (size_t)(64 * d.kb) * d.N + 32 * d.nb;
;     const unsigned voff = (unsigned)((8 * (lane & 7)) * d.N + 4 * (lane >> 3)) * 4u;
; #pragma unroll
;     for (int i = 0; i < 8; ++i)
;         __builtin_amdgcn_global_load_lds((const unsigned*)((const char*)(base + (size_t)i * d.N) + voff), (LAS unsigned*)(buf + i * 1024), 16, 0, 0);
; }
; __device__ __forceinline__ void cvt_fin(const CvtD& d, int lane, const LAS unsigned char* buf, const LAS unsigned char* shb) {
;     const int n0 = 32 * d.nb, kb = d.kb;
;     const int r0 = d.mode == 0 ? n0 + d.roff : ((n0 >> 7) * 256 + (d.mode == 2 ? 128 : 0) + (n0 & 127));
;     const int c = lane & 7, nlo = lane >> 3;
;     const LAS float* lp = (const LAS float*)buf + ((nlo >> 2) * 32 + c * 4 + (nlo & 3));
;     float v[4][8];
.LBB0_980:
	v_readlane_b32 s6, v250, 45
	v_readlane_b32 s14, v253, 39
	s_mov_b32 s10, s6
	s_mov_b32 m0, s6
	s_mul_i32 s6, s9, s14
	s_mul_hi_u32 s7, s8, s14
	s_add_i32 s7, s7, s6
	s_mul_i32 s6, s8, s14
	s_lshl_b64 s[6:7], s[6:7], 2
	s_add_u32 s6, s4, s6
	s_addc_u32 s7, s5, s7
	s_lshl_b32 s4, s11, 5
	v_lshlrev_b32_e32 v3, 3, v8
	s_ashr_i32 s5, s4, 31
	v_and_b32_e32 v7, 56, v3
	v_lshrrev_b32_e32 v4, 1, v6
	s_lshl_b64 s[4:5], s[4:5], 2
	v_mul_u32_u24_e32 v3, s14, v7
	v_and_b32_e32 v74, 28, v4
	s_add_u32 s4, s6, s4
	v_or_b32_e32 v3, v3, v74
	v_readlane_b32 s15, v253, 40
	s_addc_u32 s5, s7, s5
	v_lshlrev_b32_e32 v128, 2, v3
	v_lshl_add_u64 v[10:11], s[4:5], 0, v[128:129]
	global_load_lds_dwordx4 v128, s[4:5] nt
	s_lshl_b64 s[4:5], s[14:15], 2
	s_add_i32 s28, s10, 0x400
	v_lshl_add_u64 v[10:11], v[10:11], 0, s[4:5]
	s_mov_b32 m0, s28
	s_add_i32 s29, s10, 0x800
	global_load_lds_dwordx4 v[10:11], off nt
	v_lshl_add_u64 v[10:11], v[10:11], 0, s[4:5]
	s_mov_b32 m0, s29
	v_readlane_b32 s6, v252, 22
	global_load_lds_dwordx4 v[10:11], off nt
	v_lshl_add_u64 v[10:11], v[10:11], 0, s[4:5]
	s_mov_b32 m0, s6
	s_add_i32 s30, s10, 0x1000
	global_load_lds_dwordx4 v[10:11], off nt
	v_lshl_add_u64 v[10:11], v[10:11], 0, s[4:5]
	s_mov_b32 m0, s30
	v_readlane_b32 s6, v252, 23
	global_load_lds_dwordx4 v[10:11], off nt
	v_lshl_add_u64 v[10:11], v[10:11], 0, s[4:5]
	s_mov_b32 m0, s6
	v_readlane_b32 s6, v252, 24
	global_load_lds_dwordx4 v[10:11], off nt
	v_lshl_add_u64 v[10:11], v[10:11], 0, s[4:5]
	s_mov_b32 m0, s6
	v_and_b32_e32 v75, 7, v6
	global_load_lds_dwordx4 v[10:11], off nt
	v_lshl_add_u64 v[10:11], v[10:11], 0, s[4:5]
	v_readlane_b32 s4, v252, 25
	s_mov_b32 m0, s4
	v_readlane_b32 s4, v253, 41
	global_load_lds_dwordx4 v[10:11], off nt
	v_and_b32_e32 v6, 32, v6
	v_lshrrev_b32_e32 v10, 1, v8
	v_mov_b32_e32 v3, v129
	v_readlane_b32 s5, v253, 42
	v_lshl_add_u32 v6, v6, 2, s10
	v_lshlrev_b32_e32 v9, 4, v75
	v_and_b32_e32 v10, 12, v10
	s_mov_b32 s22, 1
	v_lshl_add_u64 v[2:3], v[2:3], 2, s[4:5]
	v_lshrrev_b32_e32 v4, 3, v8
	v_add3_u32 v76, v6, v9, v10
	v_lshlrev_b32_e32 v77, 5, v75
	v_cmp_eq_u32_e64 s[4:5], 2, v75
	v_cmp_gt_u32_e64 s[6:7], 4, v75
	v_lshlrev_b32_e32 v6, 3, v75
	v_lshlrev_b32_e32 v8, 4, v8
	v_mov_b32_e32 v9, v129
	s_mov_b64 s[10:11], 0
	v_mov_b32_e32 v78, s12
	v_mov_b32_e32 v80, s13
	v_mov_b32_e32 v79, s12
	s_branch .LBB0_984

; #define LAS __attribute__((address_space(3)))
; __device__ __forceinline__ void cvt_issue(const CvtD& d, int lane, LAS unsigned char* buf, LAS unsigned char* shb) {
;     ...
;     const float* base = d.W + (size_t)(64 * d.kb) * d.N + 32 * d.nb;
;     const unsigned voff = (unsigned)((8 * (lane & 7)) * d.N + 4 * (lane >> 3)) * 4u;
; #pragma unroll
;     for (int i = 0; i < 8; ++i)
;         __builtin_amdgcn_global_load_lds((const unsigned*)((const char*)(base + (size_t)i * d.N) + voff), (LAS unsigned*)(buf + i * 1024), 16, 0, 0);
; }
; __global__ void __launch_bounds__(NWAVES * 64, 2) mk_fwd(Args args) {
;     ...
;                         bool haveA, haveB; int rA, rB;
;                         LAS unsigned char* cb0 = lds + RING_OFF + wave * 16384; LAS unsigned char* cb1 = cb0 + 8192;
;                         LAS unsigned char* sb0 = lds + LDSCTL_OFF + 4096 + wave * 512; LAS unsigned char* sb1 = sb0 + 256;
.LBB0_1031:
	v_readlane_b32 s34, v253, 39
	s_mul_i32 s16, s19, s34
	s_mul_hi_u32 s17, s18, s34
	s_add_i32 s17, s17, s16
	s_mul_i32 s16, s18, s34
	s_lshl_b64 s[16:17], s[16:17], 2
	s_add_u32 s16, s14, s16
	s_addc_u32 s17, s15, s17
	s_lshl_b32 s14, s21, 5
	s_ashr_i32 s15, s14, 31
	s_lshl_b64 s[14:15], s[14:15], 2
	v_mul_u32_u24_e32 v10, s34, v7
	s_add_u32 s14, s16, s14
	v_or_b32_e32 v10, v10, v74
	v_readlane_b32 s16, v250, 45
	v_readlane_b32 s35, v253, 40
	s_addc_u32 s15, s17, s15
	v_lshlrev_b32_e32 v128, 2, v10
	s_add_i32 m0, s16, 0x2000
	v_lshl_add_u64 v[10:11], s[14:15], 0, v[128:129]
	global_load_lds_dwordx4 v128, s[14:15] nt
	s_lshl_b64 s[14:15], s[34:35], 2
	v_readlane_b32 s17, v252, 27
	v_lshl_add_u64 v[10:11], v[10:11], 0, s[14:15]
	s_mov_b32 m0, s17
	v_readlane_b32 s17, v252, 28
	global_load_lds_dwordx4 v[10:11], off nt
	v_lshl_add_u64 v[10:11], v[10:11], 0, s[14:15]
	s_mov_b32 m0, s17
	v_readlane_b32 s17, v252, 29
	global_load_lds_dwordx4 v[10:11], off nt
	v_lshl_add_u64 v[10:11], v[10:11], 0, s[14:15]
	s_mov_b32 m0, s17
	v_readlane_b32 s17, v252, 30
	global_load_lds_dwordx4 v[10:11], off nt
	v_lshl_add_u64 v[10:11], v[10:11], 0, s[14:15]
	s_mov_b32 m0, s17
	s_nop 0
	global_load_lds_dwordx4 v[10:11], off nt
	v_lshl_add_u64 v[10:11], v[10:11], 0, s[14:15]
	s_add_i32 m0, s16, 0x3400
	v_readlane_b32 s16, v252, 31
	global_load_lds_dwordx4 v[10:11], off nt
	v_lshl_add_u64 v[10:11], v[10:11], 0, s[14:15]
	s_mov_b32 m0, s16
	s_nop 0
	global_load_lds_dwordx4 v[10:11], off nt
	v_lshl_add_u64 v[10:11], v[10:11], 0, s[14:15]
	v_readlane_b32 s14, v252, 32
	s_mov_b32 m0, s14
	s_nop 0
	global_load_lds_dwordx4 v[10:11], off nt
	s_waitcnt vmcnt(8)
	s_and_saveexec_b64 s[14:15], s[0:1]
	s_cbranch_execz .LBB0_1033
	s_waitcnt vmcnt(0)
	v_readfirstlane_b32 s16, v5
	s_nop 1
	v_mov_b32_e32 v78, s16

; #define LAS __attribute__((address_space(3)))
; __device__ __forceinline__ void cvt_issue(const CvtD& d, int lane, LAS unsigned char* buf, LAS unsigned char* shb) {
;     ...
;     const float* base = d.W + (size_t)(64 * d.kb) * d.N + 32 * d.nb;
;     const unsigned voff = (unsigned)((8 * (lane & 7)) * d.N + 4 * (lane >> 3)) * 4u;
; #pragma unroll
;     for (int i = 0; i < 8; ++i)
;         __builtin_amdgcn_global_load_lds((const unsigned*)((const char*)(base + (size_t)i * d.N) + voff), (LAS unsigned*)(buf + i * 1024), 16, 0, 0);
; }
; __global__ void __launch_bounds__(NWAVES * 64, 2) mk_fwd(Args args) {
;     ...
;                         bool haveA, haveB; int rA, rB;
;                         LAS unsigned char* cb0 = lds + RING_OFF + wave * 16384; LAS unsigned char* cb1 = cb0 + 8192;
;                         LAS unsigned char* sb0 = lds + LDSCTL_OFF + 4096 + wave * 512; LAS unsigned char* sb1 = sb0 + 256;
.LBB0_1133:
	v_readlane_b32 s18, v250, 45
	v_readlane_b32 s34, v253, 39
	s_mov_b32 m0, s18
	s_mul_i32 s18, s21, s34
	s_mul_hi_u32 s19, s20, s34
	s_add_i32 s19, s19, s18
	s_mul_i32 s18, s20, s34
	s_lshl_b64 s[18:19], s[18:19], 2
	s_add_u32 s18, s16, s18
	s_addc_u32 s19, s17, s19
	s_lshl_b32 s16, s23, 5
	s_ashr_i32 s17, s16, 31
	s_lshl_b64 s[16:17], s[16:17], 2
	v_mul_u32_u24_e32 v10, s34, v7
	s_add_u32 s16, s18, s16
	v_or_b32_e32 v10, v10, v74
	v_readlane_b32 s35, v253, 40
	s_addc_u32 s17, s19, s17
	v_lshlrev_b32_e32 v128, 2, v10
	v_lshl_add_u64 v[10:11], s[16:17], 0, v[128:129]
	global_load_lds_dwordx4 v128, s[16:17] nt
	s_lshl_b64 s[16:17], s[34:35], 2
	v_lshl_add_u64 v[10:11], v[10:11], 0, s[16:17]
	s_mov_b32 m0, s28
	v_readlane_b32 s18, v252, 22
	global_load_lds_dwordx4 v[10:11], off nt
	v_lshl_add_u64 v[10:11], v[10:11], 0, s[16:17]
	s_mov_b32 m0, s29
	s_nop 0
	global_load_lds_dwordx4 v[10:11], off nt
	v_lshl_add_u64 v[10:11], v[10:11], 0, s[16:17]
	s_mov_b32 m0, s18
	v_readlane_b32 s18, v252, 23
	global_load_lds_dwordx4 v[10:11], off nt
	v_lshl_add_u64 v[10:11], v[10:11], 0, s[16:17]
	s_mov_b32 m0, s30
	s_nop 0
	global_load_lds_dwordx4 v[10:11], off nt
	v_lshl_add_u64 v[10:11], v[10:11], 0, s[16:17]
	s_mov_b32 m0, s18
	v_readlane_b32 s18, v252, 24
	global_load_lds_dwordx4 v[10:11], off nt
	v_lshl_add_u64 v[10:11], v[10:11], 0, s[16:17]
	s_mov_b32 m0, s18
	s_nop 0
	global_load_lds_dwordx4 v[10:11], off nt
	v_lshl_add_u64 v[10:11], v[10:11], 0, s[16:17]
	v_readlane_b32 s16, v252, 25
	s_mov_b32 m0, s16
	s_nop 0
	global_load_lds_dwordx4 v[10:11], off nt
	s_waitcnt vmcnt(8)
	s_and_saveexec_b64 s[16:17], s[0:1]
	s_cbranch_execz .LBB0_1135
	s_waitcnt vmcnt(0)
	v_readfirstlane_b32 s18, v5
	s_nop 1
	v_mov_b32_e32 v78, s18
